# re-measure: odd-slot workgroups delayed 4 x s_sleep 127 at gate GEMM start, on top of Y-prefetch + SEL optimisations
# speedup vs baseline: 1.0261x; 1.0022x over previous
;     __host__ __device__ void init(int M, int G_, int c_) { so.init(M, 1024, G_, c_); }
; __device__ __forceinline__ unsigned char* launder(unsigned char* p) { asm volatile("" : "+s"(p)); return p; }
; #define IN(i) inptr(F.lds, (i))
; #define LL launder_i(l)
; #define WSP(T, off) ((T*)(launder(args.ws) + (off)))
; __global__ void __launch_bounds__(NWAVES * 64, 2) mega_fwd(Args args) {
;     ...
;         { pg8::Gemm g{(const f16*)((const unsigned char*)xout + (size_t)64 * MiB), (const f16*)(launder(args.ws) + WS_WQG + (size_t)LL * GCOLS * 1024), MTOK, GCOLS, DM / 2}; pg8::TripleOrder S; S.init(MTOK, F.G, (int)blockIdx.x);
;           pg8::EpiGateMerge<true> E{WSP(f16, WS_R1), WSP(f16, WS_R1) + 3 * YSTR};
;           pg8::fill_tabs_q((const float*)launder(args.ws) + CW_RF, WSP(float, WS_CVEC) + (size_t)(LL * 3 + 1) * 16 * 4096, IN(I_GATEB) + LL * GCOLS, WSP(float, WS_SB) + (LL * 3 + 1) * 4096, S, TID);
;           pg8::gemm_phase<pg8::EpiGateMerge<true>, pg8::TripleOrder, true, true, true>(F.lds, g, S, E, F.wave); }
.LBB0_1138:
	s_bitcmp1_b32 s2, 3
	s_cbranch_scc0 .Lwgs_LBB01138
	s_sleep 127
	s_sleep 127
	s_sleep 127
	s_sleep 127
